# P5: leading wave-half takes its ALIGN barrier after the epilogue instead of before it (epilogue overlaps the trailing half's last MFMA segment)
# baseline (speedup 1.0000x reference)
.LBB0_566:
	s_lshl_b32 s35, s67, 10
	v_mov_b32_e32 v25, v0
	s_and_b32 s35, s35, 0x400
	s_add_i32 s35, s35, 0
	v_lshrrev_b32_e32 v26, 1, v25
	v_and_b32_e32 v162, 0x60, v26
	v_lshlrev_b32_e32 v3, 1, v25
	s_add_i32 s35, s35, 0x24cc0
	v_lshlrev_b32_e32 v2, 2, v162
	v_and_b32_e32 v3, 0x60, v3
	v_add3_u32 v14, s35, v2, v3
	ds_read_b128 v[2:5], v14
	ds_read_b128 v[6:9], v14 offset:512
	ds_read_b128 v[10:13], v14 offset:16
	v_ashrrev_i32_e32 v24, 2, v25
	s_lshl_b32 s35, s40, 10
	s_lshl_b32 s38, s38, 7
	s_waitcnt lgkmcnt(2)
	v_pk_fma_f32 v[16:17], v[4:5], s[100:101], v[228:229] op_sel_hi:[1,0,0]
	v_pk_fma_f32 v[18:19], v[2:3], s[100:101], v[228:229] op_sel_hi:[1,0,0]
	ds_read_b128 v[2:5], v14 offset:528
	s_waitcnt lgkmcnt(2)
	v_pk_fma_f32 v[20:21], v[8:9], s[72:73], 0.5 op_sel_hi:[1,0,0]
	s_waitcnt lgkmcnt(1)
	v_pk_fma_f32 v[8:9], v[12:13], s[100:101], v[228:229] op_sel_hi:[1,0,0]
	v_pk_fma_f32 v[22:23], v[6:7], s[72:73], 0.5 op_sel_hi:[1,0,0]
	v_and_b32_e32 v6, 16, v26
	s_waitcnt lgkmcnt(0)
	v_pk_fma_f32 v[14:15], v[2:3], s[72:73], 0.5 op_sel_hi:[1,0,0]
	v_and_b32_e32 v2, 15, v25
	v_pk_fma_f32 v[12:13], v[4:5], s[72:73], 0.5 op_sel_hi:[1,0,0]
	v_and_or_b32 v2, v24, s63, v2
	v_pk_fma_f32 v[4:5], v[158:159], s[98:99], v[18:19] op_sel_hi:[1,0,1] clamp
	v_lshl_add_u32 v24, s37, 8, v2
	v_pk_fma_f32 v[2:3], v[160:161], s[98:99], v[16:17] op_sel_hi:[1,0,1] clamp
	v_pk_fma_f32 v[4:5], v[4:5], s[76:77], v[230:231] op_sel_hi:[1,0,0]
	v_pk_fma_f32 v[30:31], v[2:3], s[76:77], v[230:231] op_sel_hi:[1,0,0]
	v_exp_f32_e32 v2, v4
	v_exp_f32_e32 v3, v5
	v_exp_f32_e32 v32, v30
	v_exp_f32_e32 v33, v31
	v_pk_fma_f32 v[2:3], v[2:3], s[96:97], s[96:97] op_sel_hi:[1,0,0]
	v_pk_fma_f32 v[28:29], v[154:155], s[74:75], v[22:23] op_sel_hi:[1,0,1] clamp
	v_rcp_f32_e32 v2, v2
	v_rcp_f32_e32 v3, v3
	v_pk_fma_f32 v[28:29], v[28:29], s[64:65], v[186:187] op_sel_hi:[1,0,0]
	v_pk_fma_f32 v[32:33], v[32:33], s[96:97], s[96:97] op_sel_hi:[1,0,0]
	v_pk_mul_f32 v[4:5], v[4:5], v[28:29]
	v_rcp_f32_e32 v32, v32
	v_rcp_f32_e32 v33, v33
	v_pk_mul_f32 v[4:5], v[4:5], v[2:3]
	v_pk_fma_f32 v[26:27], v[156:157], s[74:75], v[20:21] op_sel_hi:[1,0,1] clamp
	v_cvt_pk_fp8_f32 v2, v4, v5
	v_pk_fma_f32 v[26:27], v[26:27], s[64:65], v[186:187] op_sel_hi:[1,0,0]
	v_pk_mul_f32 v[4:5], v[30:31], v[26:27]
	v_pk_fma_f32 v[10:11], v[10:11], s[100:101], v[228:229] op_sel_hi:[1,0,0]
	v_pk_mul_f32 v[4:5], v[4:5], v[32:33]
	v_pk_fma_f32 v[26:27], v[150:151], s[98:99], v[10:11] op_sel_hi:[1,0,1] clamp
	v_cvt_pk_fp8_f32 v2, v4, v5 op_sel:[0,0,1]
	v_pk_fma_f32 v[4:5], v[152:153], s[98:99], v[8:9] op_sel_hi:[1,0,1] clamp
	v_pk_fma_f32 v[26:27], v[26:27], s[76:77], v[230:231] op_sel_hi:[1,0,0]
	v_pk_fma_f32 v[4:5], v[4:5], s[76:77], v[230:231] op_sel_hi:[1,0,0]
	v_pk_fma_f32 v[30:31], v[146:147], s[74:75], v[14:15] op_sel_hi:[1,0,1] clamp
	v_exp_f32_e32 v32, v26
	v_exp_f32_e32 v146, v4
	v_exp_f32_e32 v147, v5
	v_exp_f32_e32 v33, v27
	v_pk_fma_f32 v[30:31], v[30:31], s[64:65], v[186:187] op_sel_hi:[1,0,0]
	v_pk_fma_f32 v[146:147], v[146:147], s[96:97], s[96:97] op_sel_hi:[1,0,0]
	v_pk_fma_f32 v[32:33], v[32:33], s[96:97], s[96:97] op_sel_hi:[1,0,0]
	v_pk_mul_f32 v[26:27], v[26:27], v[30:31]
	v_rcp_f32_e32 v32, v32
	v_rcp_f32_e32 v33, v33
	v_rcp_f32_e32 v146, v146
	v_rcp_f32_e32 v147, v147
	v_pk_mul_f32 v[26:27], v[26:27], v[32:33]
	v_pk_fma_f32 v[28:29], v[148:149], s[74:75], v[12:13] op_sel_hi:[1,0,1] clamp
	v_cvt_pk_fp8_f32 v3, v26, v27
	v_pk_fma_f32 v[28:29], v[28:29], s[64:65], v[186:187] op_sel_hi:[1,0,0]
	v_pk_mul_f32 v[4:5], v[4:5], v[28:29]
	v_pk_fma_f32 v[26:27], v[142:143], s[98:99], v[18:19] op_sel_hi:[1,0,1] clamp
	v_pk_mul_f32 v[4:5], v[4:5], v[146:147]
	v_pk_fma_f32 v[26:27], v[26:27], s[76:77], v[230:231] op_sel_hi:[1,0,0]
	v_cvt_pk_fp8_f32 v3, v4, v5 op_sel:[0,0,1]
	v_pk_fma_f32 v[4:5], v[144:145], s[98:99], v[16:17] op_sel_hi:[1,0,1] clamp
	v_pk_fma_f32 v[32:33], v[4:5], s[76:77], v[230:231] op_sel_hi:[1,0,0]
	v_exp_f32_e32 v4, v26
	v_exp_f32_e32 v5, v27
	v_pk_fma_f32 v[30:31], v[138:139], s[74:75], v[22:23] op_sel_hi:[1,0,1] clamp
	v_exp_f32_e32 v138, v32
	v_exp_f32_e32 v139, v33
	v_pk_fma_f32 v[4:5], v[4:5], s[96:97], s[96:97] op_sel_hi:[1,0,0]
	v_pk_fma_f32 v[30:31], v[30:31], s[64:65], v[186:187] op_sel_hi:[1,0,0]
	v_rcp_f32_e32 v4, v4
	v_rcp_f32_e32 v5, v5
	v_pk_fma_f32 v[138:139], v[138:139], s[96:97], s[96:97] op_sel_hi:[1,0,0]
	v_pk_mul_f32 v[26:27], v[26:27], v[30:31]
	v_rcp_f32_e32 v138, v138
	v_rcp_f32_e32 v139, v139
	v_pk_mul_f32 v[26:27], v[26:27], v[4:5]
	v_pk_fma_f32 v[28:29], v[140:141], s[74:75], v[20:21] op_sel_hi:[1,0,1] clamp
	v_cvt_pk_fp8_f32 v4, v26, v27
	v_pk_fma_f32 v[28:29], v[28:29], s[64:65], v[186:187] op_sel_hi:[1,0,0]
	v_pk_mul_f32 v[26:27], v[32:33], v[28:29]
	v_pk_fma_f32 v[28:29], v[134:135], s[98:99], v[10:11] op_sel_hi:[1,0,1] clamp
	v_pk_mul_f32 v[26:27], v[26:27], v[138:139]
	v_pk_fma_f32 v[28:29], v[28:29], s[76:77], v[230:231] op_sel_hi:[1,0,0]
	v_cvt_pk_fp8_f32 v4, v26, v27 op_sel:[0,0,1]
	v_pk_fma_f32 v[26:27], v[136:137], s[98:99], v[8:9] op_sel_hi:[1,0,1] clamp
	v_pk_fma_f32 v[32:33], v[130:131], s[74:75], v[14:15] op_sel_hi:[1,0,1] clamp
	v_pk_fma_f32 v[26:27], v[26:27], s[76:77], v[230:231] op_sel_hi:[1,0,0]
	v_pk_fma_f32 v[30:31], v[132:133], s[74:75], v[12:13] op_sel_hi:[1,0,1] clamp
	v_exp_f32_e32 v130, v28
	v_exp_f32_e32 v132, v26
	v_exp_f32_e32 v133, v27
	v_exp_f32_e32 v131, v29
	v_pk_fma_f32 v[32:33], v[32:33], s[64:65], v[186:187] op_sel_hi:[1,0,0]
	v_pk_fma_f32 v[132:133], v[132:133], s[96:97], s[96:97] op_sel_hi:[1,0,0]
	v_pk_fma_f32 v[130:131], v[130:131], s[96:97], s[96:97] op_sel_hi:[1,0,0]
	v_pk_mul_f32 v[28:29], v[28:29], v[32:33]
	v_rcp_f32_e32 v130, v130
	v_rcp_f32_e32 v131, v131
	v_rcp_f32_e32 v132, v132
	v_rcp_f32_e32 v133, v133
	v_pk_mul_f32 v[28:29], v[28:29], v[130:131]
	v_pk_fma_f32 v[30:31], v[30:31], s[64:65], v[186:187] op_sel_hi:[1,0,0]
	v_cvt_pk_fp8_f32 v5, v28, v29
	v_pk_fma_f32 v[28:29], v[126:127], s[98:99], v[18:19] op_sel_hi:[1,0,1] clamp
	v_pk_fma_f32 v[28:29], v[28:29], s[76:77], v[230:231] op_sel_hi:[1,0,0]
	v_pk_mul_f32 v[26:27], v[26:27], v[30:31]
	v_pk_fma_f32 v[32:33], v[122:123], s[74:75], v[22:23] op_sel_hi:[1,0,1] clamp
	v_pk_mul_f32 v[26:27], v[26:27], v[132:133]
	v_exp_f32_e32 v122, v28
	v_exp_f32_e32 v123, v29
	v_cvt_pk_fp8_f32 v5, v26, v27 op_sel:[0,0,1]
	v_pk_fma_f32 v[26:27], v[128:129], s[98:99], v[16:17] op_sel_hi:[1,0,1] clamp
	v_pk_fma_f32 v[30:31], v[124:125], s[74:75], v[20:21] op_sel_hi:[1,0,1] clamp
	v_pk_fma_f32 v[26:27], v[26:27], s[76:77], v[230:231] op_sel_hi:[1,0,0]
	v_exp_f32_e32 v124, v26
	v_exp_f32_e32 v125, v27
	v_pk_fma_f32 v[122:123], v[122:123], s[96:97], s[96:97] op_sel_hi:[1,0,0]
	v_pk_fma_f32 v[32:33], v[32:33], s[64:65], v[186:187] op_sel_hi:[1,0,0]
	v_rcp_f32_e32 v122, v122
	v_rcp_f32_e32 v123, v123
	v_pk_fma_f32 v[124:125], v[124:125], s[96:97], s[96:97] op_sel_hi:[1,0,0]
	v_pk_mul_f32 v[28:29], v[28:29], v[32:33]
	v_rcp_f32_e32 v124, v124
	v_rcp_f32_e32 v125, v125
	v_pk_mul_f32 v[32:33], v[28:29], v[122:123]
	v_cvt_pk_fp8_f32 v28, v32, v33
	v_pk_fma_f32 v[30:31], v[30:31], s[64:65], v[186:187] op_sel_hi:[1,0,0]
	v_pk_mul_f32 v[26:27], v[26:27], v[30:31]
	v_pk_fma_f32 v[30:31], v[118:119], s[98:99], v[10:11] op_sel_hi:[1,0,1] clamp
	v_pk_mul_f32 v[26:27], v[26:27], v[124:125]
	v_pk_fma_f32 v[30:31], v[30:31], s[76:77], v[230:231] op_sel_hi:[1,0,0]
	v_cvt_pk_fp8_f32 v28, v26, v27 op_sel:[0,0,1]
	v_pk_fma_f32 v[26:27], v[120:121], s[98:99], v[8:9] op_sel_hi:[1,0,1] clamp
	v_pk_fma_f32 v[32:33], v[116:117], s[74:75], v[12:13] op_sel_hi:[1,0,1] clamp
	v_pk_fma_f32 v[26:27], v[26:27], s[76:77], v[230:231] op_sel_hi:[1,0,0]
	v_exp_f32_e32 v116, v30
	v_exp_f32_e32 v118, v26
	v_exp_f32_e32 v119, v27
	v_exp_f32_e32 v117, v31
	v_pk_fma_f32 v[114:115], v[114:115], s[74:75], v[14:15] op_sel_hi:[1,0,1] clamp
	v_pk_fma_f32 v[114:115], v[114:115], s[64:65], v[186:187] op_sel_hi:[1,0,0]
	v_pk_fma_f32 v[116:117], v[116:117], s[96:97], s[96:97] op_sel_hi:[1,0,0]
	v_rcp_f32_e32 v116, v116
	v_rcp_f32_e32 v117, v117
	v_pk_fma_f32 v[118:119], v[118:119], s[96:97], s[96:97] op_sel_hi:[1,0,0]
	v_pk_mul_f32 v[30:31], v[30:31], v[114:115]
	v_rcp_f32_e32 v118, v118
	v_rcp_f32_e32 v119, v119
	v_pk_mul_f32 v[30:31], v[30:31], v[116:117]
	v_pk_fma_f32 v[32:33], v[32:33], s[64:65], v[186:187] op_sel_hi:[1,0,0]
	v_cvt_pk_fp8_f32 v29, v30, v31
	v_pk_fma_f32 v[30:31], v[110:111], s[98:99], v[18:19] op_sel_hi:[1,0,1] clamp
	v_pk_fma_f32 v[30:31], v[30:31], s[76:77], v[230:231] op_sel_hi:[1,0,0]
	v_pk_mul_f32 v[26:27], v[26:27], v[32:33]
	v_pk_fma_f32 v[32:33], v[108:109], s[74:75], v[20:21] op_sel_hi:[1,0,1] clamp
	v_pk_mul_f32 v[26:27], v[26:27], v[118:119]
	v_exp_f32_e32 v108, v30
	v_exp_f32_e32 v109, v31
	v_cvt_pk_fp8_f32 v29, v26, v27 op_sel:[0,0,1]
	v_pk_fma_f32 v[26:27], v[112:113], s[98:99], v[16:17] op_sel_hi:[1,0,1] clamp
	v_pk_fma_f32 v[106:107], v[106:107], s[74:75], v[22:23] op_sel_hi:[1,0,1] clamp
	v_pk_fma_f32 v[26:27], v[26:27], s[76:77], v[230:231] op_sel_hi:[1,0,0]
	v_exp_f32_e32 v110, v26
	v_exp_f32_e32 v111, v27
	v_pk_fma_f32 v[108:109], v[108:109], s[96:97], s[96:97] op_sel_hi:[1,0,0]
	v_pk_fma_f32 v[106:107], v[106:107], s[64:65], v[186:187] op_sel_hi:[1,0,0]
	v_rcp_f32_e32 v108, v108
	v_rcp_f32_e32 v109, v109
	v_pk_fma_f32 v[110:111], v[110:111], s[96:97], s[96:97] op_sel_hi:[1,0,0]
	v_pk_mul_f32 v[30:31], v[30:31], v[106:107]
	v_rcp_f32_e32 v110, v110
	v_rcp_f32_e32 v111, v111
	v_pk_mul_f32 v[106:107], v[30:31], v[108:109]
	v_cvt_pk_fp8_f32 v30, v106, v107
	v_pk_fma_f32 v[32:33], v[32:33], s[64:65], v[186:187] op_sel_hi:[1,0,0]
	v_pk_mul_f32 v[26:27], v[26:27], v[32:33]
	v_pk_fma_f32 v[32:33], v[102:103], s[98:99], v[10:11] op_sel_hi:[1,0,1] clamp
	v_pk_mul_f32 v[26:27], v[26:27], v[110:111]
	v_pk_fma_f32 v[32:33], v[32:33], s[76:77], v[230:231] op_sel_hi:[1,0,0]
	v_cvt_pk_fp8_f32 v30, v26, v27 op_sel:[0,0,1]
	v_pk_fma_f32 v[26:27], v[104:105], s[98:99], v[8:9] op_sel_hi:[1,0,1] clamp
	v_pk_fma_f32 v[26:27], v[26:27], s[76:77], v[230:231] op_sel_hi:[1,0,0]
	v_exp_f32_e32 v102, v32
	v_exp_f32_e32 v104, v26
	v_exp_f32_e32 v105, v27
	v_exp_f32_e32 v103, v33
	v_pk_fma_f32 v[98:99], v[98:99], s[74:75], v[14:15] op_sel_hi:[1,0,1] clamp
	v_pk_fma_f32 v[98:99], v[98:99], s[64:65], v[186:187] op_sel_hi:[1,0,0]
	v_pk_fma_f32 v[102:103], v[102:103], s[96:97], s[96:97] op_sel_hi:[1,0,0]
	v_rcp_f32_e32 v102, v102
	v_rcp_f32_e32 v103, v103
	v_pk_fma_f32 v[104:105], v[104:105], s[96:97], s[96:97] op_sel_hi:[1,0,0]
	v_pk_mul_f32 v[32:33], v[32:33], v[98:99]
	v_rcp_f32_e32 v104, v104
	v_rcp_f32_e32 v105, v105
	v_pk_mul_f32 v[32:33], v[32:33], v[102:103]
	v_pk_fma_f32 v[100:101], v[100:101], s[74:75], v[12:13] op_sel_hi:[1,0,1] clamp
	v_cvt_pk_fp8_f32 v31, v32, v33
	v_pk_fma_f32 v[100:101], v[100:101], s[64:65], v[186:187] op_sel_hi:[1,0,0]
	v_pk_mul_f32 v[26:27], v[26:27], v[100:101]
	v_and_b32_e32 v25, 16, v25
	v_pk_mul_f32 v[26:27], v[26:27], v[104:105]
	s_sub_i32 s38, s38, s35
	v_cvt_pk_fp8_f32 v31, v26, v27 op_sel:[0,0,1]
	v_or_b32_e32 v26, v24, v25
	v_ashrrev_i32_e32 v27, 31, v26
	v_lshlrev_b64 v[26:27], 10, v[26:27]
	s_ashr_i32 s39, s38, 31
	v_lshl_add_u64 v[26:27], s[12:13], 0, v[26:27]
	v_lshl_add_u64 v[26:27], v[26:27], 0, s[38:39]
	v_mov_b32_e32 v7, v163
	v_lshl_add_u64 v[26:27], v[26:27], 0, v[162:163]
	v_permlane16_swap_b32_e32 v2, v4
	v_permlane16_swap_b32_e32 v3, v5
	v_lshl_add_u64 v[26:27], v[26:27], 0, v[6:7]
	global_store_dwordx4 v[26:27], v[2:5], off
	v_or_b32_e32 v26, 32, v25
	v_permlane16_swap_b32_e32 v28, v30
	v_or_b32_e32 v2, v24, v26
	v_ashrrev_i32_e32 v3, 31, v2
	v_lshlrev_b64 v[2:3], 10, v[2:3]
	v_lshl_add_u64 v[2:3], s[12:13], 0, v[2:3]
	v_lshl_add_u64 v[2:3], v[2:3], 0, s[38:39]
	v_lshl_add_u64 v[2:3], v[2:3], 0, v[162:163]
	v_permlane16_swap_b32_e32 v29, v31
	v_lshl_add_u64 v[2:3], v[2:3], 0, v[6:7]
	v_pk_fma_f32 v[4:5], v[94:95], s[98:99], v[18:19] op_sel_hi:[1,0,1] clamp
	global_store_dwordx4 v[2:3], v[28:31], off
	v_pk_fma_f32 v[2:3], v[96:97], s[98:99], v[16:17] op_sel_hi:[1,0,1] clamp
	v_pk_fma_f32 v[4:5], v[4:5], s[76:77], v[230:231] op_sel_hi:[1,0,0]
	v_pk_fma_f32 v[32:33], v[2:3], s[76:77], v[230:231] op_sel_hi:[1,0,0]
	v_exp_f32_e32 v2, v4
	v_exp_f32_e32 v3, v5
	v_pk_fma_f32 v[30:31], v[90:91], s[74:75], v[22:23] op_sel_hi:[1,0,1] clamp
	v_exp_f32_e32 v90, v32
	v_exp_f32_e32 v91, v33
	v_pk_fma_f32 v[2:3], v[2:3], s[96:97], s[96:97] op_sel_hi:[1,0,0]
	v_pk_fma_f32 v[30:31], v[30:31], s[64:65], v[186:187] op_sel_hi:[1,0,0]
	v_rcp_f32_e32 v2, v2
	v_rcp_f32_e32 v3, v3
	v_pk_fma_f32 v[28:29], v[92:93], s[74:75], v[20:21] op_sel_hi:[1,0,1] clamp
	v_pk_fma_f32 v[90:91], v[90:91], s[96:97], s[96:97] op_sel_hi:[1,0,0]
	v_pk_mul_f32 v[4:5], v[4:5], v[30:31]
	v_pk_fma_f32 v[28:29], v[28:29], s[64:65], v[186:187] op_sel_hi:[1,0,0]
	v_rcp_f32_e32 v90, v90
	v_rcp_f32_e32 v91, v91
	v_pk_mul_f32 v[4:5], v[4:5], v[2:3]
	v_cvt_pk_fp8_f32 v2, v4, v5
	v_pk_mul_f32 v[4:5], v[32:33], v[28:29]
	v_pk_fma_f32 v[28:29], v[86:87], s[98:99], v[10:11] op_sel_hi:[1,0,1] clamp
	v_pk_mul_f32 v[4:5], v[4:5], v[90:91]
	v_pk_fma_f32 v[28:29], v[28:29], s[76:77], v[230:231] op_sel_hi:[1,0,0]
	v_pk_fma_f32 v[32:33], v[82:83], s[74:75], v[14:15] op_sel_hi:[1,0,1] clamp
	v_exp_f32_e32 v82, v28
	v_cvt_pk_fp8_f32 v2, v4, v5 op_sel:[0,0,1]
	v_pk_fma_f32 v[4:5], v[88:89], s[98:99], v[8:9] op_sel_hi:[1,0,1] clamp
	v_exp_f32_e32 v83, v29
	v_pk_fma_f32 v[4:5], v[4:5], s[76:77], v[230:231] op_sel_hi:[1,0,0]
	v_pk_fma_f32 v[30:31], v[84:85], s[74:75], v[12:13] op_sel_hi:[1,0,1] clamp
	v_exp_f32_e32 v84, v4
	v_exp_f32_e32 v85, v5
	v_pk_fma_f32 v[82:83], v[82:83], s[96:97], s[96:97] op_sel_hi:[1,0,0]
	v_pk_fma_f32 v[32:33], v[32:33], s[64:65], v[186:187] op_sel_hi:[1,0,0]
	v_rcp_f32_e32 v82, v82
	v_rcp_f32_e32 v83, v83
	v_pk_fma_f32 v[84:85], v[84:85], s[96:97], s[96:97] op_sel_hi:[1,0,0]
	v_pk_mul_f32 v[28:29], v[28:29], v[32:33]
	v_rcp_f32_e32 v84, v84
	v_rcp_f32_e32 v85, v85
	v_pk_mul_f32 v[28:29], v[28:29], v[82:83]
	v_cvt_pk_fp8_f32 v3, v28, v29
	v_pk_fma_f32 v[30:31], v[30:31], s[64:65], v[186:187] op_sel_hi:[1,0,0]
	v_pk_mul_f32 v[4:5], v[4:5], v[30:31]
	v_pk_fma_f32 v[28:29], v[78:79], s[98:99], v[18:19] op_sel_hi:[1,0,1] clamp
	v_pk_mul_f32 v[4:5], v[4:5], v[84:85]
	v_pk_fma_f32 v[28:29], v[28:29], s[76:77], v[230:231] op_sel_hi:[1,0,0]
	v_cvt_pk_fp8_f32 v3, v4, v5 op_sel:[0,0,1]
	v_pk_fma_f32 v[4:5], v[80:81], s[98:99], v[16:17] op_sel_hi:[1,0,1] clamp
	v_pk_fma_f32 v[32:33], v[74:75], s[74:75], v[22:23] op_sel_hi:[1,0,1] clamp
	v_pk_fma_f32 v[74:75], v[4:5], s[76:77], v[230:231] op_sel_hi:[1,0,0]
	v_exp_f32_e32 v4, v28
	v_exp_f32_e32 v5, v29
	v_pk_fma_f32 v[30:31], v[76:77], s[74:75], v[20:21] op_sel_hi:[1,0,1] clamp
	v_exp_f32_e32 v76, v74
	v_exp_f32_e32 v77, v75
	v_pk_fma_f32 v[4:5], v[4:5], s[96:97], s[96:97] op_sel_hi:[1,0,0]
	v_pk_fma_f32 v[32:33], v[32:33], s[64:65], v[186:187] op_sel_hi:[1,0,0]
	v_rcp_f32_e32 v4, v4
	v_rcp_f32_e32 v5, v5
	v_pk_fma_f32 v[76:77], v[76:77], s[96:97], s[96:97] op_sel_hi:[1,0,0]
	v_pk_mul_f32 v[28:29], v[28:29], v[32:33]
	v_pk_fma_f32 v[30:31], v[30:31], s[64:65], v[186:187] op_sel_hi:[1,0,0]
	v_rcp_f32_e32 v76, v76
	v_rcp_f32_e32 v77, v77
	v_pk_mul_f32 v[28:29], v[28:29], v[4:5]
	v_cvt_pk_fp8_f32 v4, v28, v29
	v_pk_mul_f32 v[28:29], v[74:75], v[30:31]
	v_pk_fma_f32 v[30:31], v[70:71], s[98:99], v[10:11] op_sel_hi:[1,0,1] clamp
	v_pk_mul_f32 v[28:29], v[28:29], v[76:77]
	v_pk_fma_f32 v[30:31], v[30:31], s[76:77], v[230:231] op_sel_hi:[1,0,0]
	v_pk_fma_f32 v[32:33], v[68:69], s[74:75], v[12:13] op_sel_hi:[1,0,1] clamp
	v_exp_f32_e32 v68, v30
	v_cvt_pk_fp8_f32 v4, v28, v29 op_sel:[0,0,1]
	v_pk_fma_f32 v[28:29], v[72:73], s[98:99], v[8:9] op_sel_hi:[1,0,1] clamp
	v_exp_f32_e32 v69, v31
	v_pk_fma_f32 v[28:29], v[28:29], s[76:77], v[230:231] op_sel_hi:[1,0,0]
	v_exp_f32_e32 v70, v28
	v_exp_f32_e32 v71, v29
	v_pk_fma_f32 v[68:69], v[68:69], s[96:97], s[96:97] op_sel_hi:[1,0,0]
	v_pk_fma_f32 v[66:67], v[66:67], s[74:75], v[14:15] op_sel_hi:[1,0,1] clamp
	v_rcp_f32_e32 v68, v68
	v_rcp_f32_e32 v69, v69
	v_pk_fma_f32 v[66:67], v[66:67], s[64:65], v[186:187] op_sel_hi:[1,0,0]
	v_pk_fma_f32 v[70:71], v[70:71], s[96:97], s[96:97] op_sel_hi:[1,0,0]
	v_pk_mul_f32 v[30:31], v[30:31], v[66:67]
	v_rcp_f32_e32 v70, v70
	v_rcp_f32_e32 v71, v71
	v_pk_mul_f32 v[30:31], v[30:31], v[68:69]
	v_cvt_pk_fp8_f32 v5, v30, v31
	v_pk_fma_f32 v[32:33], v[32:33], s[64:65], v[186:187] op_sel_hi:[1,0,0]
	v_pk_mul_f32 v[28:29], v[28:29], v[32:33]
	v_pk_fma_f32 v[30:31], v[62:63], s[98:99], v[18:19] op_sel_hi:[1,0,1] clamp
	v_pk_mul_f32 v[28:29], v[28:29], v[70:71]
	v_pk_fma_f32 v[32:33], v[60:61], s[74:75], v[20:21] op_sel_hi:[1,0,1] clamp
	v_cvt_pk_fp8_f32 v5, v28, v29 op_sel:[0,0,1]
	v_pk_fma_f32 v[28:29], v[64:65], s[98:99], v[16:17] op_sel_hi:[1,0,1] clamp
	v_pk_fma_f32 v[30:31], v[30:31], s[76:77], v[230:231] op_sel_hi:[1,0,0]
	v_pk_fma_f32 v[60:61], v[28:29], s[76:77], v[230:231] op_sel_hi:[1,0,0]
	v_exp_f32_e32 v28, v30
	v_exp_f32_e32 v62, v60
	v_exp_f32_e32 v63, v61
	v_exp_f32_e32 v29, v31
	v_pk_fma_f32 v[58:59], v[58:59], s[74:75], v[22:23] op_sel_hi:[1,0,1] clamp
	v_pk_fma_f32 v[32:33], v[32:33], s[64:65], v[186:187] op_sel_hi:[1,0,0]
	v_pk_fma_f32 v[58:59], v[58:59], s[64:65], v[186:187] op_sel_hi:[1,0,0]
	v_pk_fma_f32 v[28:29], v[28:29], s[96:97], s[96:97] op_sel_hi:[1,0,0]
	v_rcp_f32_e32 v28, v28
	v_rcp_f32_e32 v29, v29
	v_pk_fma_f32 v[62:63], v[62:63], s[96:97], s[96:97] op_sel_hi:[1,0,0]
	v_pk_mul_f32 v[30:31], v[30:31], v[58:59]
	v_rcp_f32_e32 v62, v62
	v_rcp_f32_e32 v63, v63
	v_pk_mul_f32 v[30:31], v[30:31], v[28:29]
	v_cvt_pk_fp8_f32 v28, v30, v31
	v_pk_mul_f32 v[30:31], v[60:61], v[32:33]
	v_pk_fma_f32 v[32:33], v[54:55], s[98:99], v[10:11] op_sel_hi:[1,0,1] clamp
	v_pk_mul_f32 v[30:31], v[30:31], v[62:63]
	v_pk_fma_f32 v[32:33], v[32:33], s[76:77], v[230:231] op_sel_hi:[1,0,0]
	v_exp_f32_e32 v54, v32
	v_cvt_pk_fp8_f32 v28, v30, v31 op_sel:[0,0,1]
	v_pk_fma_f32 v[30:31], v[56:57], s[98:99], v[8:9] op_sel_hi:[1,0,1] clamp
	v_exp_f32_e32 v55, v33
	v_pk_fma_f32 v[30:31], v[30:31], s[76:77], v[230:231] op_sel_hi:[1,0,0]
	v_exp_f32_e32 v56, v30
	v_exp_f32_e32 v57, v31
	v_pk_fma_f32 v[54:55], v[54:55], s[96:97], s[96:97] op_sel_hi:[1,0,0]
	v_pk_fma_f32 v[50:51], v[50:51], s[74:75], v[14:15] op_sel_hi:[1,0,1] clamp
	v_rcp_f32_e32 v54, v54
	v_rcp_f32_e32 v55, v55
	v_pk_fma_f32 v[50:51], v[50:51], s[64:65], v[186:187] op_sel_hi:[1,0,0]
	v_pk_fma_f32 v[56:57], v[56:57], s[96:97], s[96:97] op_sel_hi:[1,0,0]
	v_pk_mul_f32 v[32:33], v[32:33], v[50:51]
	v_rcp_f32_e32 v56, v56
	v_rcp_f32_e32 v57, v57
	v_pk_mul_f32 v[32:33], v[32:33], v[54:55]
	v_pk_fma_f32 v[52:53], v[52:53], s[74:75], v[12:13] op_sel_hi:[1,0,1] clamp
	v_cvt_pk_fp8_f32 v29, v32, v33
	v_pk_fma_f32 v[52:53], v[52:53], s[64:65], v[186:187] op_sel_hi:[1,0,0]
	v_pk_mul_f32 v[30:31], v[30:31], v[52:53]
	v_pk_fma_f32 v[16:17], v[48:49], s[98:99], v[16:17] op_sel_hi:[1,0,1] clamp
	v_pk_fma_f32 v[18:19], v[46:47], s[98:99], v[18:19] op_sel_hi:[1,0,1] clamp
	v_pk_mul_f32 v[30:31], v[30:31], v[56:57]
	v_pk_fma_f32 v[18:19], v[18:19], s[76:77], v[230:231] op_sel_hi:[1,0,0]
	v_pk_fma_f32 v[16:17], v[16:17], s[76:77], v[230:231] op_sel_hi:[1,0,0]
	v_cvt_pk_fp8_f32 v29, v30, v31 op_sel:[0,0,1]
	v_exp_f32_e32 v30, v18
	v_exp_f32_e32 v32, v16
	v_exp_f32_e32 v33, v17
	v_exp_f32_e32 v31, v19
	v_pk_fma_f32 v[22:23], v[42:43], s[74:75], v[22:23] op_sel_hi:[1,0,1] clamp
	v_pk_fma_f32 v[20:21], v[44:45], s[74:75], v[20:21] op_sel_hi:[1,0,1] clamp
	v_pk_fma_f32 v[22:23], v[22:23], s[64:65], v[186:187] op_sel_hi:[1,0,0]
	v_pk_fma_f32 v[30:31], v[30:31], s[96:97], s[96:97] op_sel_hi:[1,0,0]
	v_rcp_f32_e32 v30, v30
	v_rcp_f32_e32 v31, v31
	v_pk_fma_f32 v[32:33], v[32:33], s[96:97], s[96:97] op_sel_hi:[1,0,0]
	v_pk_mul_f32 v[18:19], v[18:19], v[22:23]
	v_rcp_f32_e32 v32, v32
	v_rcp_f32_e32 v33, v33
	v_pk_mul_f32 v[18:19], v[18:19], v[30:31]
	v_cvt_pk_fp8_f32 v30, v18, v19
	v_pk_fma_f32 v[20:21], v[20:21], s[64:65], v[186:187] op_sel_hi:[1,0,0]
	v_pk_mul_f32 v[16:17], v[16:17], v[20:21]
	v_pk_fma_f32 v[10:11], v[38:39], s[98:99], v[10:11] op_sel_hi:[1,0,1] clamp
	v_pk_mul_f32 v[16:17], v[16:17], v[32:33]
	v_pk_fma_f32 v[10:11], v[10:11], s[76:77], v[230:231] op_sel_hi:[1,0,0]
	v_cvt_pk_fp8_f32 v30, v16, v17 op_sel:[0,0,1]
	v_exp_f32_e32 v16, v10
	v_exp_f32_e32 v17, v11
	v_pk_fma_f32 v[8:9], v[40:41], s[98:99], v[8:9] op_sel_hi:[1,0,1] clamp
	v_pk_fma_f32 v[14:15], v[34:35], s[74:75], v[14:15] op_sel_hi:[1,0,1] clamp
	v_pk_fma_f32 v[8:9], v[8:9], s[76:77], v[230:231] op_sel_hi:[1,0,0]
	v_exp_f32_e32 v18, v8
	v_exp_f32_e32 v19, v9
	v_pk_fma_f32 v[16:17], v[16:17], s[96:97], s[96:97] op_sel_hi:[1,0,0]
	v_pk_fma_f32 v[14:15], v[14:15], s[64:65], v[186:187] op_sel_hi:[1,0,0]
	v_rcp_f32_e32 v16, v16
	v_rcp_f32_e32 v17, v17
	v_pk_fma_f32 v[18:19], v[18:19], s[96:97], s[96:97] op_sel_hi:[1,0,0]
	v_pk_mul_f32 v[10:11], v[10:11], v[14:15]
	v_rcp_f32_e32 v18, v18
	v_rcp_f32_e32 v19, v19
	v_pk_mul_f32 v[10:11], v[10:11], v[16:17]
	v_pk_fma_f32 v[12:13], v[36:37], s[74:75], v[12:13] op_sel_hi:[1,0,1] clamp
	v_cvt_pk_fp8_f32 v31, v10, v11
	v_pk_fma_f32 v[12:13], v[12:13], s[64:65], v[186:187] op_sel_hi:[1,0,0]
	v_pk_mul_f32 v[8:9], v[8:9], v[12:13]
	v_add_u32_e32 v10, 0x80, v24
	v_pk_mul_f32 v[8:9], v[8:9], v[18:19]
	v_permlane16_swap_b32_e32 v2, v4
	v_cvt_pk_fp8_f32 v31, v8, v9 op_sel:[0,0,1]
	v_or_b32_e32 v8, v10, v25
	v_ashrrev_i32_e32 v9, 31, v8
	v_lshlrev_b64 v[8:9], 10, v[8:9]
	v_lshl_add_u64 v[8:9], s[12:13], 0, v[8:9]
	v_lshl_add_u64 v[8:9], v[8:9], 0, s[38:39]
	v_lshl_add_u64 v[8:9], v[8:9], 0, v[162:163]
	v_permlane16_swap_b32_e32 v3, v5
	v_lshl_add_u64 v[8:9], v[8:9], 0, v[6:7]
	global_store_dwordx4 v[8:9], v[2:5], off
	v_permlane16_swap_b32_e32 v28, v30
	s_nop 0
	v_or_b32_e32 v2, v10, v26
	v_ashrrev_i32_e32 v3, 31, v2
	v_lshlrev_b64 v[2:3], 10, v[2:3]
	v_lshl_add_u64 v[2:3], s[12:13], 0, v[2:3]
	v_lshl_add_u64 v[2:3], v[2:3], 0, s[38:39]
	v_lshl_add_u64 v[2:3], v[2:3], 0, v[162:163]
	v_permlane16_swap_b32_e32 v29, v31
	v_lshl_add_u64 v[2:3], v[2:3], 0, v[6:7]
	s_andn2_b64 vcc, exec, s[26:27]
	s_cbranch_vccnz .Lal5_skip
	s_barrier
.Lal5_skip:
	s_and_b64 vcc, exec, s[4:5]
	s_mov_b64 s[4:5], -1
	global_store_dwordx4 v[2:3], v[28:31], off
	s_cbranch_vccnz .LBB0_557
	s_andn2_b64 vcc, exec, s[16:17]
	s_cbranch_vccnz .LBB0_569
	s_lshl_b32 s4, s66, 10
	s_and_b32 s4, s4, 0x400
	s_add_i32 s4, s4, 0
	s_ashr_i32 s37, s36, 31
	s_add_i32 s35, s4, 0x24cc0
	s_lshl_b64 s[4:5], s[36:37], 13
	s_add_u32 s37, s14, s4
	s_addc_u32 s38, s15, s5
	s_lshl_b32 s4, s36, 10
	s_lshl_b32 s5, s34, 7
	s_sub_i32 s4, s5, s4
	s_ashr_i32 s5, s4, 31
	s_lshl_b64 s[4:5], s[4:5], 2
	s_add_u32 s4, s37, s4
	s_addc_u32 s5, s38, s5
	s_mov_b32 m0, s35
	s_nop 0
	global_load_lds_dwordx4 v178, s[4:5] offset:0
